# adds: norm2 row pass issues all 12 loads of a trip before the first wait (global_ loads, counted vmcnt); layer-0 out-proj epilogue prefetches the 16 residual loads of a half
# speedup vs baseline: 1.0213x; 1.0027x over previous
; __device__ __forceinline__ u32x4 pack8(f32x4 a, f32x4 b) { u32x4 w; w.x = pk2(a[0], a[1]); w.y = pk2(a[2], a[3]); w.z = pk2(b[0], b[1]); w.w = pk2(b[2], b[3]); return w; }
; __device__ __forceinline__ f32x2 rtab_get(LAS unsigned char* lds, int ui, int r) { return ((const LAS f32x2*)(lds + RTAB_OFF))[(ui & 1) * 256 + r]; }
;     __device__ __forceinline__ void operator()(const f32x4 (&acc)[2][2][4][2], const Unit& u, int ui, int wr, int wc, int fr, int fq, LAS unsigned char* lds) const {
;     ...
;             if (xin) {
; #pragma unroll
;                 for (int m = 0; m < 4; ++m) { const int r = ai * 128 + wr * 64 + m * 16 + fr, row = u.pm * 256 + r; const float rm = rtab_get(lds, ui, r)[1];
; #pragma unroll
;                     for (int bj = 0; bj < 2; ++bj) { const size_t o = (size_t)row * DM + u.pn * 256 + bj * 128 + wc * 32 + fq * 8;
;                         const f32x4 a = *(const f32x4*)(xin + o), b = *(const f32x4*)(xin + o + 4);
;                         *(u32x4*)(hout + o) = pack8(a + acc[ai][bj][m][0] * rm, b + acc[ai][bj][m][1] * rm); }
;                     asm volatile("" ::: "memory"); }
.LBB0_961:
	v_mov_b32_e32 v130, v188
	s_lshl_b32 s7, s7, 3
	v_and_b32_e32 v0, 15, v130
	s_lshl_b32 s42, s6, 8
	v_or_b32_e32 v131, s53, v0
	s_lshl_b32 s3, s3, 8
	s_add_i32 s7, s7, 0
	s_ashr_i32 s43, s42, 31
	v_lshrrev_b32_e32 v130, 1, v130
	s_add_i32 s39, s7, 0x22400
	s_or_b64 s[6:7], s[42:43], s[28:29]
	v_and_b32_e32 v130, 24, v130
	v_cndmask_b32_e64 v132, 0, 1, s[36:37]
	v_add_u32_e32 v162, s3, v131
	v_or_b32_e32 v158, s6, v130
	v_mov_b32_e32 v159, s7
	v_cmp_ne_u32_e64 s[14:15], 1, v132
	s_andn2_b64 vcc, exec, s[36:37]
	v_lshl_add_u32 v175, v131, 3, s39
	v_ashrrev_i32_e32 v163, 31, v162
	v_add_u32_e32 v168, 16, v162
	v_add_u32_e32 v166, 32, v162
	v_add_u32_e32 v164, 48, v162
	v_readlane_b32 s61, v255, 16
	s_cbranch_vccnz .LBB0_963
	v_ashrrev_i32_e32 v169, 31, v168
	v_ashrrev_i32_e32 v167, 31, v166
	v_ashrrev_i32_e32 v165, 31, v164
	s_mov_b64 s[46:47], 0
	v_lshlrev_b64 v[132:133], 10, v[162:163]
	v_lshl_add_u64 v[142:143], v[132:133], 0, v[158:159]
	v_lshl_add_u64 v[144:145], v[142:143], 2, s[22:23]
	global_load_dwordx4 v[244:247], v[144:145], off offset:16
	global_load_dwordx4 v[176:179], v[144:145], off
	global_load_dwordx4 v[180:183], v[144:145], off offset:528
	global_load_dwordx4 v[184:187], v[144:145], off offset:512
	v_lshlrev_b64 v[132:133], 10, v[168:169]
	v_lshl_add_u64 v[142:143], v[132:133], 0, v[158:159]
	v_lshl_add_u64 v[144:145], v[142:143], 2, s[22:23]
	global_load_dwordx4 v[190:193], v[144:145], off offset:16
	global_load_dwordx4 v[194:197], v[144:145], off
	global_load_dwordx4 v[198:201], v[144:145], off offset:528
	global_load_dwordx4 v[202:205], v[144:145], off offset:512
	v_lshlrev_b64 v[132:133], 10, v[166:167]
	v_lshl_add_u64 v[142:143], v[132:133], 0, v[158:159]
	v_lshl_add_u64 v[144:145], v[142:143], 2, s[22:23]
	global_load_dwordx4 v[206:209], v[144:145], off offset:16
	global_load_dwordx4 v[210:213], v[144:145], off
	global_load_dwordx4 v[214:217], v[144:145], off offset:528
	global_load_dwordx4 v[218:221], v[144:145], off offset:512
	v_lshlrev_b64 v[132:133], 10, v[164:165]
	v_lshl_add_u64 v[142:143], v[132:133], 0, v[158:159]
	v_lshl_add_u64 v[144:145], v[142:143], 2, s[22:23]
	global_load_dwordx4 v[222:225], v[144:145], off offset:16
	global_load_dwordx4 v[226:229], v[144:145], off
	global_load_dwordx4 v[230:233], v[144:145], off offset:528
	global_load_dwordx4 v[240:243], v[144:145], off offset:512
	ds_read_b64 v[140:141], v175 offset:0
	v_lshlrev_b64 v[132:133], 10, v[162:163]
	v_lshl_add_u64 v[142:143], v[132:133], 0, v[158:159]
	v_lshlrev_b64 v[142:143], 1, v[142:143]
	s_waitcnt vmcnt(14) lgkmcnt(0)
	v_pk_fma_f32 v[146:147], v[124:125], v[140:141], v[246:247] op_sel:[0,1,0]
	v_pk_fma_f32 v[138:139], v[128:129], v[140:141], v[178:179] op_sel:[0,1,0]
	v_pk_fma_f32 v[136:137], v[126:127], v[140:141], v[176:177] op_sel:[0,1,0]
	v_pk_fma_f32 v[134:135], v[122:123], v[140:141], v[244:245] op_sel:[0,1,0]
	v_cvt_pk_bf16_f32 v132, v136, v137
	v_cvt_pk_bf16_f32 v133, v138, v139
	v_cvt_pk_bf16_f32 v134, v134, v135
	v_cvt_pk_bf16_f32 v135, v146, v147
	v_lshl_add_u64 v[136:137], s[26:27], 0, v[142:143]
	global_store_dwordx4 v[136:137], v[132:135], off
	s_nop 1
	v_or_b32_e32 v142, 0x100, v142
	s_waitcnt vmcnt(13)
	v_pk_fma_f32 v[146:147], v[116:117], v[140:141], v[182:183] op_sel:[0,1,0]
	v_pk_fma_f32 v[138:139], v[120:121], v[140:141], v[186:187] op_sel:[0,1,0]
	v_pk_fma_f32 v[136:137], v[118:119], v[140:141], v[184:185] op_sel:[0,1,0]
	v_pk_fma_f32 v[134:135], v[114:115], v[140:141], v[180:181] op_sel:[0,1,0]
	v_cvt_pk_bf16_f32 v132, v136, v137
	v_cvt_pk_bf16_f32 v133, v138, v139
	v_cvt_pk_bf16_f32 v134, v134, v135
	v_cvt_pk_bf16_f32 v135, v146, v147
	v_lshl_add_u64 v[136:137], s[26:27], 0, v[142:143]
	global_store_dwordx4 v[136:137], v[132:135], off
	s_nop 1
	ds_read_b64 v[140:141], v175 offset:128
	v_lshlrev_b64 v[132:133], 10, v[168:169]
	v_lshl_add_u64 v[142:143], v[132:133], 0, v[158:159]
	v_lshlrev_b64 v[142:143], 1, v[142:143]
	s_waitcnt vmcnt(12) lgkmcnt(0)
; __device__ __forceinline__ u32x4 pack8(f32x4 a, f32x4 b) { u32x4 w; w.x = pk2(a[0], a[1]); w.y = pk2(a[2], a[3]); w.z = pk2(b[0], b[1]); w.w = pk2(b[2], b[3]); return w; }
; __device__ __forceinline__ f32x2 rtab_get(LAS unsigned char* lds, int ui, int r) { return ((const LAS f32x2*)(lds + RTAB_OFF))[(ui & 1) * 256 + r]; }
;     __device__ __forceinline__ void operator()(const f32x4 (&acc)[2][2][4][2], const Unit& u, int ui, int wr, int wc, int fr, int fq, LAS unsigned char* lds) const {
;     ...
;             if (xin) {
; #pragma unroll
;                 for (int m = 0; m < 4; ++m) { const int r = ai * 128 + wr * 64 + m * 16 + fr, row = u.pm * 256 + r; const float rm = rtab_get(lds, ui, r)[1];
; #pragma unroll
;                     for (int bj = 0; bj < 2; ++bj) { const size_t o = (size_t)row * DM + u.pn * 256 + bj * 128 + wc * 32 + fq * 8;
;                         const f32x4 a = *(const f32x4*)(xin + o), b = *(const f32x4*)(xin + o + 4);
;                         *(u32x4*)(hout + o) = pack8(a + acc[ai][bj][m][0] * rm, b + acc[ai][bj][m][1] * rm); }
;                     asm volatile("" ::: "memory"); }
	v_pk_fma_f32 v[146:147], v[108:109], v[140:141], v[192:193] op_sel:[0,1,0]
	v_pk_fma_f32 v[138:139], v[112:113], v[140:141], v[196:197] op_sel:[0,1,0]
	v_pk_fma_f32 v[136:137], v[110:111], v[140:141], v[194:195] op_sel:[0,1,0]
	v_pk_fma_f32 v[134:135], v[106:107], v[140:141], v[190:191] op_sel:[0,1,0]
	v_cvt_pk_bf16_f32 v132, v136, v137
	v_cvt_pk_bf16_f32 v133, v138, v139
	v_cvt_pk_bf16_f32 v134, v134, v135
	v_cvt_pk_bf16_f32 v135, v146, v147
	v_lshl_add_u64 v[136:137], s[26:27], 0, v[142:143]
	global_store_dwordx4 v[136:137], v[132:135], off
	s_nop 1
	v_or_b32_e32 v142, 0x100, v142
	s_waitcnt vmcnt(11)
	v_pk_fma_f32 v[146:147], v[100:101], v[140:141], v[200:201] op_sel:[0,1,0]
	v_pk_fma_f32 v[138:139], v[104:105], v[140:141], v[204:205] op_sel:[0,1,0]
	v_pk_fma_f32 v[136:137], v[102:103], v[140:141], v[202:203] op_sel:[0,1,0]
	v_pk_fma_f32 v[134:135], v[98:99], v[140:141], v[198:199] op_sel:[0,1,0]
	v_cvt_pk_bf16_f32 v132, v136, v137
	v_cvt_pk_bf16_f32 v133, v138, v139
	v_cvt_pk_bf16_f32 v134, v134, v135
	v_cvt_pk_bf16_f32 v135, v146, v147
	v_lshl_add_u64 v[136:137], s[26:27], 0, v[142:143]
	global_store_dwordx4 v[136:137], v[132:135], off
	s_nop 1
	ds_read_b64 v[140:141], v175 offset:256
	v_lshlrev_b64 v[132:133], 10, v[166:167]
	v_lshl_add_u64 v[142:143], v[132:133], 0, v[158:159]
	v_lshlrev_b64 v[142:143], 1, v[142:143]
	s_waitcnt vmcnt(10) lgkmcnt(0)
	v_pk_fma_f32 v[146:147], v[92:93], v[140:141], v[208:209] op_sel:[0,1,0]
	v_pk_fma_f32 v[138:139], v[96:97], v[140:141], v[212:213] op_sel:[0,1,0]
	v_pk_fma_f32 v[136:137], v[94:95], v[140:141], v[210:211] op_sel:[0,1,0]
	v_pk_fma_f32 v[134:135], v[90:91], v[140:141], v[206:207] op_sel:[0,1,0]
	v_cvt_pk_bf16_f32 v132, v136, v137
	v_cvt_pk_bf16_f32 v133, v138, v139
	v_cvt_pk_bf16_f32 v134, v134, v135
	v_cvt_pk_bf16_f32 v135, v146, v147
	v_lshl_add_u64 v[136:137], s[26:27], 0, v[142:143]
	global_store_dwordx4 v[136:137], v[132:135], off
	s_nop 1
	v_or_b32_e32 v142, 0x100, v142
	s_waitcnt vmcnt(9)
	v_pk_fma_f32 v[146:147], v[84:85], v[140:141], v[216:217] op_sel:[0,1,0]
	v_pk_fma_f32 v[138:139], v[88:89], v[140:141], v[220:221] op_sel:[0,1,0]
	v_pk_fma_f32 v[136:137], v[86:87], v[140:141], v[218:219] op_sel:[0,1,0]
	v_pk_fma_f32 v[134:135], v[82:83], v[140:141], v[214:215] op_sel:[0,1,0]
	v_cvt_pk_bf16_f32 v132, v136, v137
	v_cvt_pk_bf16_f32 v133, v138, v139
	v_cvt_pk_bf16_f32 v134, v134, v135
	v_cvt_pk_bf16_f32 v135, v146, v147
	v_lshl_add_u64 v[136:137], s[26:27], 0, v[142:143]
	global_store_dwordx4 v[136:137], v[132:135], off
	s_nop 1
	ds_read_b64 v[140:141], v175 offset:384
	v_lshlrev_b64 v[132:133], 10, v[164:165]
	v_lshl_add_u64 v[142:143], v[132:133], 0, v[158:159]
	v_lshlrev_b64 v[142:143], 1, v[142:143]
	s_waitcnt vmcnt(8) lgkmcnt(0)
	v_pk_fma_f32 v[146:147], v[76:77], v[140:141], v[224:225] op_sel:[0,1,0]
	v_pk_fma_f32 v[138:139], v[80:81], v[140:141], v[228:229] op_sel:[0,1,0]
	v_pk_fma_f32 v[136:137], v[78:79], v[140:141], v[226:227] op_sel:[0,1,0]
	v_pk_fma_f32 v[134:135], v[74:75], v[140:141], v[222:223] op_sel:[0,1,0]
	v_cvt_pk_bf16_f32 v132, v136, v137
	v_cvt_pk_bf16_f32 v133, v138, v139
	v_cvt_pk_bf16_f32 v134, v134, v135
	v_cvt_pk_bf16_f32 v135, v146, v147
	v_lshl_add_u64 v[136:137], s[26:27], 0, v[142:143]
	global_store_dwordx4 v[136:137], v[132:135], off
	s_nop 1
	v_or_b32_e32 v142, 0x100, v142
	s_waitcnt vmcnt(7)
	v_pk_fma_f32 v[146:147], v[68:69], v[140:141], v[232:233] op_sel:[0,1,0]
	v_pk_fma_f32 v[138:139], v[72:73], v[140:141], v[242:243] op_sel:[0,1,0]
	v_pk_fma_f32 v[136:137], v[70:71], v[140:141], v[240:241] op_sel:[0,1,0]
	v_pk_fma_f32 v[134:135], v[66:67], v[140:141], v[230:231] op_sel:[0,1,0]
	v_cvt_pk_bf16_f32 v132, v136, v137
	v_cvt_pk_bf16_f32 v133, v138, v139
	v_cvt_pk_bf16_f32 v134, v134, v135
	v_cvt_pk_bf16_f32 v135, v146, v147
	v_lshl_add_u64 v[136:137], s[26:27], 0, v[142:143]
	global_store_dwordx4 v[136:137], v[132:135], off
	s_nop 1
	s_branch .LBB0_964

; __device__ __forceinline__ u32x4 pack8(f32x4 a, f32x4 b) { u32x4 w; w.x = pk2(a[0], a[1]); w.y = pk2(a[2], a[3]); w.z = pk2(b[0], b[1]); w.w = pk2(b[2], b[3]); return w; }
; __device__ __forceinline__ f32x2 rtab_get(LAS unsigned char* lds, int ui, int r) { return ((const LAS f32x2*)(lds + RTAB_OFF))[(ui & 1) * 256 + r]; }
;     __device__ __forceinline__ void operator()(const f32x4 (&acc)[2][2][4][2], const Unit& u, int ui, int wr, int wc, int fr, int fq, LAS unsigned char* lds) const {
;     ...
;             if (xin) {
; #pragma unroll
;                 for (int m = 0; m < 4; ++m) { const int r = ai * 128 + wr * 64 + m * 16 + fr, row = u.pm * 256 + r; const float rm = rtab_get(lds, ui, r)[1];
; #pragma unroll
;                     for (int bj = 0; bj < 2; ++bj) { const size_t o = (size_t)row * DM + u.pn * 256 + bj * 128 + wc * 32 + fq * 8;
;                         const f32x4 a = *(const f32x4*)(xin + o), b = *(const f32x4*)(xin + o + 4);
;                         *(u32x4*)(hout + o) = pack8(a + acc[ai][bj][m][0] * rm, b + acc[ai][bj][m][1] * rm); }
;                     asm volatile("" ::: "memory"); }
.LBB0_966:
	s_and_b64 vcc, exec, s[14:15]
	v_add_u32_e32 v96, 0x80, v162
	v_add_u32_e32 v94, 0x90, v162
	v_add_u32_e32 v92, 0xa0, v162
	v_add_u32_e32 v90, 0xb0, v162
	s_cbranch_vccnz .LBB0_974
	v_ashrrev_i32_e32 v97, 31, v96
	v_ashrrev_i32_e32 v95, 31, v94
	v_ashrrev_i32_e32 v93, 31, v92
	v_ashrrev_i32_e32 v91, 31, v90
	v_lshlrev_b64 v[66:67], 10, v[96:97]
	v_lshl_add_u64 v[76:77], v[66:67], 0, v[158:159]
	v_lshl_add_u64 v[78:79], v[76:77], 2, s[22:23]
	global_load_dwordx4 v[244:247], v[78:79], off offset:16
	global_load_dwordx4 v[176:179], v[78:79], off
	global_load_dwordx4 v[180:183], v[78:79], off offset:528
	global_load_dwordx4 v[184:187], v[78:79], off offset:512
	v_lshlrev_b64 v[66:67], 10, v[94:95]
	v_lshl_add_u64 v[76:77], v[66:67], 0, v[158:159]
	v_lshl_add_u64 v[78:79], v[76:77], 2, s[22:23]
	global_load_dwordx4 v[190:193], v[78:79], off offset:16
	global_load_dwordx4 v[194:197], v[78:79], off
	global_load_dwordx4 v[198:201], v[78:79], off offset:528
	global_load_dwordx4 v[202:205], v[78:79], off offset:512
	v_lshlrev_b64 v[66:67], 10, v[92:93]
	v_lshl_add_u64 v[76:77], v[66:67], 0, v[158:159]
	v_lshl_add_u64 v[78:79], v[76:77], 2, s[22:23]
	global_load_dwordx4 v[206:209], v[78:79], off offset:16
	global_load_dwordx4 v[210:213], v[78:79], off
	global_load_dwordx4 v[214:217], v[78:79], off offset:528
	global_load_dwordx4 v[218:221], v[78:79], off offset:512
	v_lshlrev_b64 v[66:67], 10, v[90:91]
	v_lshl_add_u64 v[76:77], v[66:67], 0, v[158:159]
	v_lshl_add_u64 v[78:79], v[76:77], 2, s[22:23]
	global_load_dwordx4 v[222:225], v[78:79], off offset:16
	global_load_dwordx4 v[226:229], v[78:79], off
	global_load_dwordx4 v[230:233], v[78:79], off offset:528
	global_load_dwordx4 v[240:243], v[78:79], off offset:512
	ds_read_b64 v[74:75], v175 offset:1024
	v_lshlrev_b64 v[66:67], 10, v[96:97]
	v_lshl_add_u64 v[76:77], v[66:67], 0, v[158:159]
	v_lshlrev_b64 v[76:77], 1, v[76:77]
	s_waitcnt vmcnt(14) lgkmcnt(0)
	v_pk_fma_f32 v[80:81], v[60:61], v[74:75], v[246:247] op_sel:[0,1,0]
	v_pk_fma_f32 v[72:73], v[64:65], v[74:75], v[178:179] op_sel:[0,1,0]
	v_pk_fma_f32 v[70:71], v[62:63], v[74:75], v[176:177] op_sel:[0,1,0]
	v_pk_fma_f32 v[68:69], v[58:59], v[74:75], v[244:245] op_sel:[0,1,0]
	v_cvt_pk_bf16_f32 v66, v70, v71
	v_cvt_pk_bf16_f32 v67, v72, v73
	v_cvt_pk_bf16_f32 v68, v68, v69
	v_cvt_pk_bf16_f32 v69, v80, v81
	v_lshl_add_u64 v[70:71], s[26:27], 0, v[76:77]
	global_store_dwordx4 v[70:71], v[66:69], off
	s_nop 1
	v_or_b32_e32 v76, 0x100, v76
	s_waitcnt vmcnt(13)
	v_pk_fma_f32 v[80:81], v[52:53], v[74:75], v[182:183] op_sel:[0,1,0]
	v_pk_fma_f32 v[72:73], v[56:57], v[74:75], v[186:187] op_sel:[0,1,0]
	v_pk_fma_f32 v[70:71], v[54:55], v[74:75], v[184:185] op_sel:[0,1,0]
	v_pk_fma_f32 v[68:69], v[50:51], v[74:75], v[180:181] op_sel:[0,1,0]
	v_cvt_pk_bf16_f32 v66, v70, v71
	v_cvt_pk_bf16_f32 v67, v72, v73
	v_cvt_pk_bf16_f32 v68, v68, v69
	v_cvt_pk_bf16_f32 v69, v80, v81
	v_lshl_add_u64 v[70:71], s[26:27], 0, v[76:77]
	global_store_dwordx4 v[70:71], v[66:69], off
	s_nop 1
	ds_read_b64 v[74:75], v175 offset:1152
	v_lshlrev_b64 v[66:67], 10, v[94:95]
	v_lshl_add_u64 v[76:77], v[66:67], 0, v[158:159]
	v_lshlrev_b64 v[76:77], 1, v[76:77]
	s_waitcnt vmcnt(12) lgkmcnt(0)
	v_pk_fma_f32 v[80:81], v[44:45], v[74:75], v[192:193] op_sel:[0,1,0]
	v_pk_fma_f32 v[72:73], v[48:49], v[74:75], v[196:197] op_sel:[0,1,0]
	v_pk_fma_f32 v[70:71], v[46:47], v[74:75], v[194:195] op_sel:[0,1,0]
	v_pk_fma_f32 v[68:69], v[42:43], v[74:75], v[190:191] op_sel:[0,1,0]
	v_cvt_pk_bf16_f32 v66, v70, v71
	v_cvt_pk_bf16_f32 v67, v72, v73
	v_cvt_pk_bf16_f32 v68, v68, v69
	v_cvt_pk_bf16_f32 v69, v80, v81
	v_lshl_add_u64 v[70:71], s[26:27], 0, v[76:77]
	global_store_dwordx4 v[70:71], v[66:69], off
	s_nop 1
	v_or_b32_e32 v76, 0x100, v76
	s_waitcnt vmcnt(11)
	v_pk_fma_f32 v[80:81], v[36:37], v[74:75], v[200:201] op_sel:[0,1,0]
	v_pk_fma_f32 v[72:73], v[40:41], v[74:75], v[204:205] op_sel:[0,1,0]
	v_pk_fma_f32 v[70:71], v[38:39], v[74:75], v[202:203] op_sel:[0,1,0]
	v_pk_fma_f32 v[68:69], v[34:35], v[74:75], v[198:199] op_sel:[0,1,0]
	v_cvt_pk_bf16_f32 v66, v70, v71
	v_cvt_pk_bf16_f32 v67, v72, v73
	v_cvt_pk_bf16_f32 v68, v68, v69
	v_cvt_pk_bf16_f32 v69, v80, v81
	v_lshl_add_u64 v[70:71], s[26:27], 0, v[76:77]
	global_store_dwordx4 v[70:71], v[66:69], off
	s_nop 1
	ds_read_b64 v[74:75], v175 offset:1280
	v_lshlrev_b64 v[66:67], 10, v[92:93]
	v_lshl_add_u64 v[76:77], v[66:67], 0, v[158:159]
	v_lshlrev_b64 v[76:77], 1, v[76:77]
	s_waitcnt vmcnt(10) lgkmcnt(0)
	v_pk_fma_f32 v[80:81], v[28:29], v[74:75], v[208:209] op_sel:[0,1,0]
	v_pk_fma_f32 v[72:73], v[32:33], v[74:75], v[212:213] op_sel:[0,1,0]
	v_pk_fma_f32 v[70:71], v[30:31], v[74:75], v[210:211] op_sel:[0,1,0]
	v_pk_fma_f32 v[68:69], v[26:27], v[74:75], v[206:207] op_sel:[0,1,0]
	v_cvt_pk_bf16_f32 v66, v70, v71
	v_cvt_pk_bf16_f32 v67, v72, v73
	v_cvt_pk_bf16_f32 v68, v68, v69
	v_cvt_pk_bf16_f32 v69, v80, v81
	v_lshl_add_u64 v[70:71], s[26:27], 0, v[76:77]
	global_store_dwordx4 v[70:71], v[66:69], off
	s_nop 1
	v_or_b32_e32 v76, 0x100, v76
	s_waitcnt vmcnt(9)
	v_pk_fma_f32 v[80:81], v[20:21], v[74:75], v[216:217] op_sel:[0,1,0]
	v_pk_fma_f32 v[72:73], v[24:25], v[74:75], v[220:221] op_sel:[0,1,0]
	v_pk_fma_f32 v[70:71], v[22:23], v[74:75], v[218:219] op_sel:[0,1,0]
	v_pk_fma_f32 v[68:69], v[18:19], v[74:75], v[214:215] op_sel:[0,1,0]
	v_cvt_pk_bf16_f32 v66, v70, v71
	v_cvt_pk_bf16_f32 v67, v72, v73
	v_cvt_pk_bf16_f32 v68, v68, v69
	v_cvt_pk_bf16_f32 v69, v80, v81
	v_lshl_add_u64 v[70:71], s[26:27], 0, v[76:77]
	global_store_dwordx4 v[70:71], v[66:69], off
	s_nop 1
	ds_read_b64 v[74:75], v175 offset:1408
	v_lshlrev_b64 v[66:67], 10, v[90:91]
	v_lshl_add_u64 v[76:77], v[66:67], 0, v[158:159]
	v_lshlrev_b64 v[76:77], 1, v[76:77]
	s_waitcnt vmcnt(8) lgkmcnt(0)
	v_pk_fma_f32 v[80:81], v[12:13], v[74:75], v[224:225] op_sel:[0,1,0]
	v_pk_fma_f32 v[72:73], v[16:17], v[74:75], v[228:229] op_sel:[0,1,0]
	v_pk_fma_f32 v[70:71], v[14:15], v[74:75], v[226:227] op_sel:[0,1,0]
	v_pk_fma_f32 v[68:69], v[10:11], v[74:75], v[222:223] op_sel:[0,1,0]
	v_cvt_pk_bf16_f32 v66, v70, v71
	v_cvt_pk_bf16_f32 v67, v72, v73
	v_cvt_pk_bf16_f32 v68, v68, v69
	v_cvt_pk_bf16_f32 v69, v80, v81
	v_lshl_add_u64 v[70:71], s[26:27], 0, v[76:77]
	global_store_dwordx4 v[70:71], v[66:69], off
	s_nop 1
	v_or_b32_e32 v76, 0x100, v76
	s_waitcnt vmcnt(7)
	v_pk_fma_f32 v[80:81], v[4:5], v[74:75], v[232:233] op_sel:[0,1,0]
	v_pk_fma_f32 v[72:73], v[8:9], v[74:75], v[242:243] op_sel:[0,1,0]
	v_pk_fma_f32 v[70:71], v[6:7], v[74:75], v[240:241] op_sel:[0,1,0]
	v_pk_fma_f32 v[68:69], v[2:3], v[74:75], v[230:231] op_sel:[0,1,0]
	v_cvt_pk_bf16_f32 v66, v70, v71
	v_cvt_pk_bf16_f32 v67, v72, v73
	v_cvt_pk_bf16_f32 v68, v68, v69
	v_cvt_pk_bf16_f32 v69, v80, v81
	v_lshl_add_u64 v[70:71], s[26:27], 0, v[76:77]
	global_store_dwordx4 v[70:71], v[66:69], off
	s_nop 1
	s_cbranch_execnz .LBB0_969

; __device__ __forceinline__ unsigned pk2(float lo, float hi) { f32x2_cv_ v = {lo, hi}; return __builtin_bit_cast(unsigned, __builtin_convertvector(v, bf16x2_cv_)); }
; __device__ __forceinline__ void phase_norm2(Frame& F, int l, float ysc) {
;     ...
;     for (int row0 = 2 * F.gw(); row0 < T; row0 += 2 * F.ngw()) {
;         u32x4 hw[2][2], ya[2][2], yb[2][2];
; #pragma unroll
;         for (int q = 0; q < 2; ++q) { const u32x4* xr = (const u32x4*)(HB + (size_t)(row0 + q) * DM) + F.lane; const u32x4* y0 = (const u32x4*)(Y + (size_t)(row0 + q) * 2 * DM) + F.lane; const u32x4* y1 = y0 + DM / 8;
; #pragma unroll
;             for (int j = 0; j < 2; ++j) { hw[q][j] = xr[64 * j]; ya[q][j] = y0[64 * j]; yb[q][j] = y1[64 * j]; } }
; #pragma unroll
;         for (int q = 0; q < 2; ++q) { float s = 0.f; u32x4* xr = (u32x4*)(HB + (size_t)(row0 + q) * DM) + F.lane;
; #pragma unroll
;             for (int j = 0; j < 2; ++j) { float h[8], a[8], b[8]; unpack8(hw[q][j], h); unpack8(ya[q][j], a); unpack8(yb[q][j], b);
; #pragma unroll
;                 for (int i = 0; i < 8; ++i) h[i] += ysc * (a[i] + b[i]);
;                 const u32x4 o = (u32x4){pk2(h[0], h[1]), pk2(h[2], h[3]), pk2(h[4], h[5]), pk2(h[6], h[7])}; xr[64 * j] = o;
;                 unpack8(o, h);
; #pragma unroll
;                 for (int i = 0; i < 8; i += 4) s += (h[i] * h[i] + h[i + 1] * h[i + 1]) + (h[i + 2] * h[i + 2] + h[i + 3] * h[i + 3]); }
;             s = wave_sum(s);
;             if (F.lane == 0) RS[row0 + q] = 1.0f / sqrtf(s * (1.f / DM) + EPS); }
.LBB0_1421:
	v_lshl_add_u64 v[42:43], s[74:75], 0, v[40:41]
	v_add_co_u32_e32 v44, vcc, 0xee00000, v42
	v_lshl_add_u64 v[2:3], s[74:75], 0, v[38:39]
	s_nop 0
	v_addc_co_u32_e32 v45, vcc, 0, v43, vcc
	global_load_dwordx4 v[46:49], v[44:45], off
	v_add_co_u32_e32 v4, vcc, 0x15200000, v2
	s_mov_b32 s3, 0x15201000
	s_nop 0
	v_addc_co_u32_e32 v5, vcc, 0, v3, vcc
	global_load_dwordx4 v[50:53], v[4:5], off
	global_load_dwordx4 v[54:57], v[4:5], off offset:2048
	global_load_dwordx4 v[26:29], v[44:45], off offset:1024
	global_load_dwordx4 v[34:37], v[4:5], off offset:1024
	global_load_dwordx4 v[30:33], v[4:5], off offset:3072
	global_load_dwordx4 v[14:17], v[44:45], off offset:2048
	v_add_co_u32_e32 v10, vcc, s3, v2
	s_nop 1
	v_addc_co_u32_e32 v11, vcc, 0, v3, vcc
	global_load_dwordx4 v[22:25], v[10:11], off
	global_load_dwordx4 v[18:21], v[10:11], off offset:2048
	global_load_dwordx4 v[2:5], v[44:45], off offset:3072
	global_load_dwordx4 v[6:9], v[10:11], off offset:1024
	s_nop 0
	global_load_dwordx4 v[10:13], v[10:11], off offset:3072
	s_waitcnt vmcnt(6)
	v_lshlrev_b32_e32 v58, 16, v46
	v_lshlrev_b32_e32 v60, 16, v50
	v_and_b32_e32 v61, 0xffff0000, v50
	v_lshlrev_b32_e32 v62, 16, v54
	v_and_b32_e32 v63, 0xffff0000, v54
	v_and_b32_e32 v59, 0xffff0000, v46
	v_pk_add_f32 v[60:61], v[60:61], v[62:63]
	v_lshlrev_b32_e32 v50, 16, v51
	v_and_b32_e32 v51, 0xffff0000, v51
	v_lshlrev_b32_e32 v54, 16, v55
	v_and_b32_e32 v55, 0xffff0000, v55
	v_pk_add_f32 v[58:59], v[60:61], v[58:59]
	v_lshlrev_b32_e32 v46, 16, v47
	v_and_b32_e32 v47, 0xffff0000, v47
	v_pk_add_f32 v[50:51], v[50:51], v[54:55]
	v_lshlrev_b32_e32 v54, 16, v52
	v_and_b32_e32 v55, 0xffff0000, v52
	v_lshlrev_b32_e32 v60, 16, v56
	v_and_b32_e32 v61, 0xffff0000, v56
	v_pk_add_f32 v[50:51], v[50:51], v[46:47]
	v_lshlrev_b32_e32 v46, 16, v48
	v_and_b32_e32 v47, 0xffff0000, v48
	v_pk_add_f32 v[54:55], v[54:55], v[60:61]
	v_lshlrev_b32_e32 v48, 16, v53
	v_pk_add_f32 v[54:55], v[54:55], v[46:47]
	v_lshlrev_b32_e32 v46, 16, v49
	v_and_b32_e32 v47, 0xffff0000, v49
	v_and_b32_e32 v49, 0xffff0000, v53
	v_lshlrev_b32_e32 v52, 16, v57
	v_and_b32_e32 v53, 0xffff0000, v57
	v_pk_add_f32 v[48:49], v[48:49], v[52:53]
	s_nop 0
	v_pk_add_f32 v[52:53], v[48:49], v[46:47]
	v_cvt_pk_bf16_f32 v46, v58, v59
	v_cvt_pk_bf16_f32 v47, v50, v51
	v_cvt_pk_bf16_f32 v48, v54, v55
	v_cvt_pk_bf16_f32 v49, v52, v53
	global_store_dwordx4 v[44:45], v[46:49], off
	v_lshlrev_b32_e32 v0, 16, v46
	v_lshlrev_b32_e32 v50, 16, v47
	v_and_b32_e32 v46, 0xffff0000, v46
	v_and_b32_e32 v47, 0xffff0000, v47
	v_mul_f32_e32 v46, v46, v46
	v_fmac_f32_e32 v46, v0, v0
	v_mul_f32_e32 v0, v47, v47
	v_lshlrev_b32_e32 v51, 16, v48
	v_and_b32_e32 v48, 0xffff0000, v48
	v_lshlrev_b32_e32 v52, 16, v49
	v_and_b32_e32 v49, 0xffff0000, v49
	v_fmac_f32_e32 v0, v50, v50
	v_add_f32_e32 v0, v46, v0
	v_mul_f32_e32 v46, v48, v48
	v_mul_f32_e32 v47, v49, v49
	v_fmac_f32_e32 v46, v51, v51
	v_fmac_f32_e32 v47, v52, v52
	v_add_f32_e32 v46, v46, v47
	v_lshlrev_b32_e32 v48, 16, v34
	v_and_b32_e32 v49, 0xffff0000, v34
	v_lshlrev_b32_e32 v50, 16, v30
	v_and_b32_e32 v51, 0xffff0000, v30
	v_add_f32_e32 v0, v0, v46
	v_lshlrev_b32_e32 v46, 16, v26
	v_and_b32_e32 v47, 0xffff0000, v26
	v_pk_add_f32 v[48:49], v[48:49], v[50:51]
	v_lshlrev_b32_e32 v34, 16, v35
	v_and_b32_e32 v35, 0xffff0000, v35
	v_lshlrev_b32_e32 v30, 16, v31
	v_and_b32_e32 v31, 0xffff0000, v31
	v_pk_add_f32 v[46:47], v[48:49], v[46:47]
	v_lshlrev_b32_e32 v26, 16, v27
	v_and_b32_e32 v27, 0xffff0000, v27
	v_pk_add_f32 v[30:31], v[34:35], v[30:31]
	v_lshlrev_b32_e32 v34, 16, v36
	v_and_b32_e32 v35, 0xffff0000, v36
	v_lshlrev_b32_e32 v48, 16, v32
	v_and_b32_e32 v49, 0xffff0000, v32
	v_pk_add_f32 v[30:31], v[30:31], v[26:27]
	v_lshlrev_b32_e32 v26, 16, v28
	v_and_b32_e32 v27, 0xffff0000, v28
	v_pk_add_f32 v[34:35], v[34:35], v[48:49]
	v_lshlrev_b32_e32 v28, 16, v37
	v_pk_add_f32 v[34:35], v[34:35], v[26:27]
	v_lshlrev_b32_e32 v26, 16, v29
	v_and_b32_e32 v27, 0xffff0000, v29
	v_and_b32_e32 v29, 0xffff0000, v37
	v_lshlrev_b32_e32 v32, 16, v33
	v_and_b32_e32 v33, 0xffff0000, v33
	v_pk_add_f32 v[28:29], v[28:29], v[32:33]
	s_nop 0
	v_pk_add_f32 v[32:33], v[28:29], v[26:27]
	v_cvt_pk_bf16_f32 v26, v46, v47
	v_cvt_pk_bf16_f32 v27, v30, v31
	v_cvt_pk_bf16_f32 v28, v34, v35
	v_cvt_pk_bf16_f32 v29, v32, v33
	global_store_dwordx4 v[44:45], v[26:29], off offset:1024
	v_lshlrev_b32_e32 v30, 16, v26
	v_lshlrev_b32_e32 v31, 16, v27
	v_and_b32_e32 v26, 0xffff0000, v26
	v_and_b32_e32 v27, 0xffff0000, v27
	v_mul_f32_e32 v26, v26, v26
	v_mul_f32_e32 v27, v27, v27
	v_fmac_f32_e32 v26, v30, v30
	v_fmac_f32_e32 v27, v31, v31
	v_lshlrev_b32_e32 v32, 16, v28
	v_and_b32_e32 v28, 0xffff0000, v28
	v_lshlrev_b32_e32 v33, 16, v29
	v_and_b32_e32 v29, 0xffff0000, v29
	v_add_f32_e32 v26, v26, v27
	v_add_f32_e32 v0, v0, v26
	v_mul_f32_e32 v26, v28, v28
	v_mul_f32_e32 v27, v29, v29
	v_fmac_f32_e32 v26, v32, v32
	v_fmac_f32_e32 v27, v33, v33
	v_add_f32_e32 v26, v26, v27
	v_add_f32_e32 v0, v26, v0
	s_nop 1
	v_add_f32_dpp v0, v0, v0 quad_perm:[1,0,3,2] row_mask:0xf bank_mask:0xf bound_ctrl:1
	s_nop 1
	v_add_f32_dpp v0, v0, v0 quad_perm:[2,3,0,1] row_mask:0xf bank_mask:0xf bound_ctrl:1
	s_nop 1
	v_add_f32_dpp v0, v0, v0 row_half_mirror row_mask:0xf bank_mask:0xf bound_ctrl:1
	s_nop 1
	v_add_f32_dpp v0, v0, v0 row_mirror row_mask:0xf bank_mask:0xf bound_ctrl:1
	s_nop 0
	v_readlane_b32 s12, v0, 0
	v_readlane_b32 s3, v0, 16
	v_readlane_b32 s13, v0, 32
	v_readlane_b32 s6, v0, 48
	s_and_saveexec_b64 s[16:17], s[10:11]
	s_cbranch_execz .LBB0_1423
	v_mov_b32_e32 v26, s3
	v_mov_b32_e32 v27, s6
	v_pk_add_f32 v[26:27], s[12:13], v[26:27]
	s_mov_b32 s3, 0xf800000
	v_add_f32_e32 v0, v26, v27
	v_fmamk_f32 v0, v0, 0x3a800000, v236
	v_mul_f32_e32 v26, 0x4f800000, v0
	v_cmp_gt_f32_e32 vcc, s3, v0
	s_add_u32 s3, s74, s14
	s_nop 0
	v_cndmask_b32_e32 v0, v0, v26, vcc
	v_sqrt_f32_e32 v26, v0
	s_nop 0
	v_add_u32_e32 v27, -1, v26
	v_fma_f32 v28, -v27, v26, v0
	v_cmp_ge_f32_e64 s[12:13], 0, v28
	v_add_u32_e32 v28, 1, v26
	s_nop 0
	v_cndmask_b32_e64 v27, v26, v27, s[12:13]
	v_fma_f32 v26, -v28, v26, v0
	v_cmp_lt_f32_e64 s[12:13], 0, v26
	s_nop 1
	v_cndmask_b32_e64 v26, v27, v28, s[12:13]
	v_mul_f32_e32 v27, 0x37800000, v26
	v_cndmask_b32_e32 v26, v26, v27, vcc
	v_cmp_class_f32_e32 vcc, v0, v251
	s_nop 1
	v_cndmask_b32_e32 v0, v26, v0, vcc
	v_div_scale_f32 v26, s[6:7], v0, v0, 1.0
	v_rcp_f32_e32 v27, v26
	s_addc_u32 s6, s75, s15
	v_fma_f32 v28, -v26, v27, 1.0
	v_fmac_f32_e32 v27, v28, v27
	v_div_scale_f32 v28, vcc, 1.0, v0, 1.0
	v_mul_f32_e32 v29, v28, v27
	v_fma_f32 v30, -v26, v29, v28
	v_fmac_f32_e32 v29, v30, v27
	v_fma_f32 v26, -v26, v29, v28
	v_div_fmas_f32 v26, v26, v27, v29
	v_div_fixup_f32 v0, v26, v0, 1.0
	v_mov_b32_e32 v26, s3
	v_add_co_u32_e32 v26, vcc, 0x500000, v26
	v_mov_b32_e32 v27, s6
	s_nop 0
	v_addc_co_u32_e32 v27, vcc, 0, v27, vcc
	global_store_dword v[26:27], v0, off
; __device__ __forceinline__ unsigned pk2(float lo, float hi) { f32x2_cv_ v = {lo, hi}; return __builtin_bit_cast(unsigned, __builtin_convertvector(v, bf16x2_cv_)); }
; __device__ __forceinline__ void phase_norm2(Frame& F, int l, float ysc) {
;     ...
;         for (int q = 0; q < 2; ++q) { float s = 0.f; u32x4* xr = (u32x4*)(HB + (size_t)(row0 + q) * DM) + F.lane;
; #pragma unroll
;             for (int j = 0; j < 2; ++j) { float h[8], a[8], b[8]; unpack8(hw[q][j], h); unpack8(ya[q][j], a); unpack8(yb[q][j], b);
; #pragma unroll
;                 for (int i = 0; i < 8; ++i) h[i] += ysc * (a[i] + b[i]);
;                 const u32x4 o = (u32x4){pk2(h[0], h[1]), pk2(h[2], h[3]), pk2(h[4], h[5]), pk2(h[6], h[7])}; xr[64 * j] = o;
;                 unpack8(o, h);
; #pragma unroll
;                 for (int i = 0; i < 8; i += 4) s += (h[i] * h[i] + h[i + 1] * h[i + 1]) + (h[i + 2] * h[i + 2] + h[i + 3] * h[i + 3]); }
;             s = wave_sum(s);
;             if (F.lane == 0) RS[row0 + q] = 1.0f / sqrtf(s * (1.f / DM) + EPS); }
.LBB0_1423:
	s_or_b64 exec, exec, s[16:17]
	s_waitcnt vmcnt(3)
	v_lshlrev_b32_e32 v32, 16, v22
	v_and_b32_e32 v33, 0xffff0000, v22
	v_lshlrev_b32_e32 v34, 16, v18
	v_and_b32_e32 v35, 0xffff0000, v18
	v_lshlrev_b32_e32 v30, 16, v14
	v_and_b32_e32 v31, 0xffff0000, v14
	v_pk_add_f32 v[32:33], v[32:33], v[34:35]
	v_lshlrev_b32_e32 v22, 16, v23
	v_and_b32_e32 v23, 0xffff0000, v23
	v_lshlrev_b32_e32 v18, 16, v19
	v_and_b32_e32 v19, 0xffff0000, v19
	v_pk_add_f32 v[30:31], v[32:33], v[30:31]
	v_lshlrev_b32_e32 v14, 16, v15
	v_and_b32_e32 v15, 0xffff0000, v15
	v_pk_add_f32 v[18:19], v[22:23], v[18:19]
	v_lshlrev_b32_e32 v22, 16, v24
	v_and_b32_e32 v23, 0xffff0000, v24
	v_lshlrev_b32_e32 v32, 16, v20
	v_and_b32_e32 v33, 0xffff0000, v20
	v_pk_add_f32 v[18:19], v[18:19], v[14:15]
	v_lshlrev_b32_e32 v14, 16, v16
	v_and_b32_e32 v15, 0xffff0000, v16
	v_pk_add_f32 v[22:23], v[22:23], v[32:33]
	v_lshlrev_b32_e32 v16, 16, v25
	v_pk_add_f32 v[22:23], v[22:23], v[14:15]
	v_lshlrev_b32_e32 v14, 16, v17
	v_and_b32_e32 v15, 0xffff0000, v17
	v_and_b32_e32 v17, 0xffff0000, v25
	v_lshlrev_b32_e32 v20, 16, v21
	v_and_b32_e32 v21, 0xffff0000, v21
	v_pk_add_f32 v[16:17], v[16:17], v[20:21]
	s_mov_b64 s[6:7], 0xee00800
	v_pk_add_f32 v[20:21], v[16:17], v[14:15]
	v_lshl_add_u64 v[26:27], v[42:43], 0, s[6:7]
	v_cvt_pk_bf16_f32 v14, v30, v31
	v_cvt_pk_bf16_f32 v15, v18, v19
	v_cvt_pk_bf16_f32 v16, v22, v23
	v_cvt_pk_bf16_f32 v17, v20, v21
	global_store_dwordx4 v[26:27], v[14:17], off
	v_lshlrev_b32_e32 v0, 16, v14
	v_lshlrev_b32_e32 v18, 16, v15
	v_and_b32_e32 v14, 0xffff0000, v14
	v_and_b32_e32 v15, 0xffff0000, v15
	v_mul_f32_e32 v14, v14, v14
	v_fmac_f32_e32 v14, v0, v0
	v_mul_f32_e32 v0, v15, v15
	v_lshlrev_b32_e32 v19, 16, v16
	v_and_b32_e32 v16, 0xffff0000, v16
	v_lshlrev_b32_e32 v20, 16, v17
	v_and_b32_e32 v17, 0xffff0000, v17
	v_fmac_f32_e32 v0, v18, v18
	v_add_f32_e32 v0, v14, v0
	v_mul_f32_e32 v14, v16, v16
	v_mul_f32_e32 v15, v17, v17
	v_fmac_f32_e32 v14, v19, v19
	v_fmac_f32_e32 v15, v20, v20
	v_add_f32_e32 v14, v14, v15
	v_lshlrev_b32_e32 v16, 16, v6
	v_and_b32_e32 v17, 0xffff0000, v6
	v_lshlrev_b32_e32 v18, 16, v10
	v_and_b32_e32 v19, 0xffff0000, v10
	v_add_f32_e32 v0, v0, v14
	v_lshlrev_b32_e32 v14, 16, v2
	v_and_b32_e32 v15, 0xffff0000, v2
	v_pk_add_f32 v[16:17], v[16:17], v[18:19]
	v_lshlrev_b32_e32 v6, 16, v7
	v_and_b32_e32 v7, 0xffff0000, v7
	v_lshlrev_b32_e32 v10, 16, v11
	v_and_b32_e32 v11, 0xffff0000, v11
	v_pk_add_f32 v[14:15], v[16:17], v[14:15]
	v_lshlrev_b32_e32 v2, 16, v3
	v_and_b32_e32 v3, 0xffff0000, v3
	v_pk_add_f32 v[6:7], v[6:7], v[10:11]
	v_lshlrev_b32_e32 v10, 16, v8
	v_and_b32_e32 v11, 0xffff0000, v8
	v_lshlrev_b32_e32 v16, 16, v12
	v_and_b32_e32 v17, 0xffff0000, v12
	v_pk_add_f32 v[6:7], v[6:7], v[2:3]
	v_lshlrev_b32_e32 v2, 16, v4
	v_and_b32_e32 v3, 0xffff0000, v4
	v_pk_add_f32 v[10:11], v[10:11], v[16:17]
	v_lshlrev_b32_e32 v4, 16, v9
	v_pk_add_f32 v[10:11], v[10:11], v[2:3]
	v_lshlrev_b32_e32 v2, 16, v5
	v_and_b32_e32 v3, 0xffff0000, v5
	v_and_b32_e32 v5, 0xffff0000, v9
	v_lshlrev_b32_e32 v8, 16, v13
	v_and_b32_e32 v9, 0xffff0000, v13
	v_pk_add_f32 v[4:5], v[4:5], v[8:9]
	s_mov_b64 s[6:7], 0xee00c00
	v_pk_add_f32 v[8:9], v[4:5], v[2:3]
	v_lshl_add_u64 v[28:29], v[42:43], 0, s[6:7]
	v_cvt_pk_bf16_f32 v2, v14, v15
	v_cvt_pk_bf16_f32 v3, v6, v7
	v_cvt_pk_bf16_f32 v4, v10, v11
	v_cvt_pk_bf16_f32 v5, v8, v9
	global_store_dwordx4 v[28:29], v[2:5], off
	v_lshlrev_b32_e32 v6, 16, v2
	v_lshlrev_b32_e32 v7, 16, v3
	v_and_b32_e32 v2, 0xffff0000, v2
	v_and_b32_e32 v3, 0xffff0000, v3
	v_mul_f32_e32 v2, v2, v2
	v_mul_f32_e32 v3, v3, v3
	v_fmac_f32_e32 v2, v6, v6
	v_fmac_f32_e32 v3, v7, v7
	v_lshlrev_b32_e32 v8, 16, v4
	v_and_b32_e32 v4, 0xffff0000, v4
	v_lshlrev_b32_e32 v9, 16, v5
	v_and_b32_e32 v5, 0xffff0000, v5
	v_add_f32_e32 v2, v2, v3
	v_add_f32_e32 v0, v0, v2
	v_mul_f32_e32 v2, v4, v4
	v_mul_f32_e32 v3, v5, v5
	v_fmac_f32_e32 v2, v8, v8
	v_fmac_f32_e32 v3, v9, v9
	v_add_f32_e32 v2, v2, v3
	v_add_f32_e32 v0, v2, v0
	s_nop 1
	v_add_f32_dpp v0, v0, v0 quad_perm:[1,0,3,2] row_mask:0xf bank_mask:0xf bound_ctrl:1
	s_nop 1
	v_add_f32_dpp v0, v0, v0 quad_perm:[2,3,0,1] row_mask:0xf bank_mask:0xf bound_ctrl:1
	s_nop 1
	v_add_f32_dpp v0, v0, v0 row_half_mirror row_mask:0xf bank_mask:0xf bound_ctrl:1
	s_nop 1
	v_add_f32_dpp v0, v0, v0 row_mirror row_mask:0xf bank_mask:0xf bound_ctrl:1
	s_nop 0
	v_readlane_b32 s12, v0, 0
	v_readlane_b32 s3, v0, 16
	v_readlane_b32 s13, v0, 32
	v_readlane_b32 s6, v0, 48
	s_and_saveexec_b64 s[16:17], s[10:11]
	s_cbranch_execz .LBB0_1420
	v_mov_b32_e32 v2, s3
	v_mov_b32_e32 v3, s6
	v_pk_add_f32 v[2:3], s[12:13], v[2:3]
	s_mov_b32 s3, 0xf800000
	v_add_f32_e32 v0, v2, v3
	v_fmamk_f32 v0, v0, 0x3a800000, v236
	v_mul_f32_e32 v2, 0x4f800000, v0
	v_cmp_gt_f32_e32 vcc, s3, v0
	s_add_u32 s3, s74, s14
	s_nop 0
	v_cndmask_b32_e32 v0, v0, v2, vcc
	v_sqrt_f32_e32 v2, v0
	s_nop 0
	v_add_u32_e32 v3, -1, v2
	v_fma_f32 v4, -v3, v2, v0
	v_cmp_ge_f32_e64 s[12:13], 0, v4
	v_add_u32_e32 v4, 1, v2
	s_nop 0
	v_cndmask_b32_e64 v3, v2, v3, s[12:13]
	v_fma_f32 v2, -v4, v2, v0
	v_cmp_lt_f32_e64 s[12:13], 0, v2
	s_nop 1
	v_cndmask_b32_e64 v2, v3, v4, s[12:13]
	v_mul_f32_e32 v3, 0x37800000, v2
	v_cndmask_b32_e32 v2, v2, v3, vcc
	v_cmp_class_f32_e32 vcc, v0, v251
	s_nop 1
	v_cndmask_b32_e32 v0, v2, v0, vcc
	v_div_scale_f32 v2, s[6:7], v0, v0, 1.0
	v_rcp_f32_e32 v3, v2
	s_addc_u32 s6, s75, s15
	v_fma_f32 v4, -v2, v3, 1.0
	v_fmac_f32_e32 v3, v4, v3
	v_div_scale_f32 v4, vcc, 1.0, v0, 1.0
	v_mul_f32_e32 v5, v4, v3
	v_fma_f32 v6, -v2, v5, v4
	v_fmac_f32_e32 v5, v6, v3
	v_fma_f32 v2, -v2, v5, v4
	v_div_fmas_f32 v2, v2, v3, v5
	v_div_fixup_f32 v0, v2, v0, 1.0
	v_mov_b32_e32 v2, s3
	v_add_co_u32_e32 v2, vcc, 0x500000, v2
	v_mov_b32_e32 v3, s6
	s_nop 0
	v_addc_co_u32_e32 v3, vcc, 0, v3, vcc
	global_store_dword v[2:3], v0, off offset:4
	s_branch .LBB0_1420
